# bias-init LDS reads issued right after the partial-sum write (before the barrier, counted wait lets them stay in flight)
# speedup vs baseline: 1.0034x; 1.0034x over previous
.LBB1_4:
	s_and_saveexec_b64 s[8:9], s[2:3]
	v_perm_b32 v5, v1, v102, s23
	v_perm_b32 v9, v121, v103, s23
	s_or_b64 exec, exec, s[8:9]
	v_mov_b32_e32 v144, v1
	v_mov_b32_e32 v145, v121
	v_mfma_f32_16x16x32_f16 v[164:167], v[30:33], v[2:5], 0
	v_mfma_f32_16x16x32_f16 v[180:183], v[22:25], v[2:5], 0
	s_cmp_lg_u32 s22, 0x818000
	v_permlane32_swap_b32_e32 v1, v144
	v_permlane32_swap_b32_e32 v121, v145
	v_mfma_f32_16x16x32_f16 v[168:171], v[30:33], v[6:9], 0
	v_mfma_f32_16x16x32_f16 v[184:187], v[22:25], v[6:9], 0
	s_cselect_b32 s9, s11, 15
	s_and_saveexec_b64 s[32:33], s[2:3]
	v_perm_b32 v17, v144, v115, s23
	v_perm_b32 v29, v145, v116, s23
	s_or_b64 exec, exec, s[32:33]
	v_mfma_f32_16x16x32_f16 v[172:175], v[30:33], v[14:17], 0
	v_mfma_f32_16x16x32_f16 v[188:191], v[22:25], v[14:17], 0
	v_mfma_f32_16x16x32_f16 v[176:179], v[30:33], v[26:29], 0
	v_mfma_f32_16x16x32_f16 v[192:195], v[22:25], v[26:29], 0
	v_mfma_f32_16x16x32_f16 v[208:211], v[18:21], v[2:5], 0
	v_mfma_f32_16x16x32_f16 v[224:227], v[10:13], v[2:5], 0
	v_cvt_pk_f16_f32 v122, v164, v165
	v_cvt_pk_f16_f32 v123, v166, v167
	v_pk_max_f16 v122, v122, 0
	v_pk_max_f16 v123, v123, 0
	v_cvt_pk_f16_f32 v124, v180, v181
	v_cvt_pk_f16_f32 v125, v182, v183
	v_pk_max_f16 v124, v124, 0
	v_pk_max_f16 v125, v125, 0
	ds_write_b128 v107, v[122:125]
	v_mfma_f32_16x16x32_f16 v[212:215], v[18:21], v[6:9], 0
	v_mfma_f32_16x16x32_f16 v[228:231], v[10:13], v[6:9], 0
	v_cvt_pk_f16_f32 v126, v168, v169
	v_cvt_pk_f16_f32 v127, v170, v171
	v_pk_max_f16 v126, v126, 0
	v_pk_max_f16 v127, v127, 0
	v_cvt_pk_f16_f32 v128, v184, v185
	v_cvt_pk_f16_f32 v129, v186, v187
	v_pk_max_f16 v128, v128, 0
	v_pk_max_f16 v129, v129, 0
	ds_write_b128 v107, v[126:129] offset:16384
	v_mfma_f32_16x16x32_f16 v[216:219], v[18:21], v[14:17], 0
	v_mfma_f32_16x16x32_f16 v[232:235], v[10:13], v[14:17], 0
	v_cvt_pk_f16_f32 v134, v172, v173
	v_cvt_pk_f16_f32 v135, v174, v175
	v_pk_max_f16 v134, v134, 0
	v_pk_max_f16 v135, v135, 0
	v_cvt_pk_f16_f32 v136, v188, v189
	v_cvt_pk_f16_f32 v137, v190, v191
	v_pk_max_f16 v136, v136, 0
	v_pk_max_f16 v137, v137, 0
	ds_write_b128 v107, v[134:137] offset:32768
	v_mfma_f32_16x16x32_f16 v[220:223], v[18:21], v[26:29], 0
	v_mfma_f32_16x16x32_f16 v[236:239], v[10:13], v[26:29], 0
	v_cvt_pk_f16_f32 v138, v176, v177
	v_cvt_pk_f16_f32 v139, v178, v179
	v_pk_max_f16 v138, v138, 0
	v_pk_max_f16 v139, v139, 0
	v_cvt_pk_f16_f32 v140, v192, v193
	v_cvt_pk_f16_f32 v141, v194, v195
	v_pk_max_f16 v140, v140, 0
	v_pk_max_f16 v141, v141, 0
	ds_write_b128 v107, v[138:141] offset:49152
	v_add_u32_e32 v111, s64, v111
	v_add_u32_e32 v98, s65, v98
	s_lshl_b32 s20, s9, 7
	v_lshl_add_u64 v[0:1], s[20:21], 3, v[132:133]
	s_add_i32 s25, s22, s34
	s_lshl_b32 s8, s9, 8
	buffer_load_dwordx4 v[192:195], v147, s[16:19], s25 offen
	buffer_load_dwordx4 v[196:199], v148, s[16:19], s25 offen
	buffer_load_dwordx4 v[200:203], v149, s[16:19], s25 offen
	buffer_load_dwordx4 v[204:207], v150, s[16:19], s25 offen
	s_waitcnt vmcnt(19) lgkmcnt(4)
	v_mfma_f32_16x16x32_f16 v[164:167], v[58:61], v[122:125], v[240:243]
	s_load_dword s30, s[12:13], 0x0
	v_cvt_pk_f16_f32 v142, v208, v209
	v_cvt_pk_f16_f32 v143, v210, v211
	v_mfma_f32_16x16x32_f16 v[168:171], v[58:61], v[126:129], v[240:243]
	v_pk_max_f16 v142, v142, 0
	v_pk_max_f16 v143, v143, 0
	v_mfma_f32_16x16x32_f16 v[172:175], v[58:61], v[134:137], v[240:243]
	v_cvt_pk_f16_f32 v144, v224, v225
	v_cvt_pk_f16_f32 v145, v226, v227
	v_mfma_f32_16x16x32_f16 v[10:13], v[58:61], v[138:141], v[240:243]
	v_pk_max_f16 v144, v144, 0
	v_pk_max_f16 v145, v145, 0
	ds_write_b128 v108, v[142:145]
	s_waitcnt vmcnt(18)
	v_mfma_f32_16x16x32_f16 v[58:61], v[54:57], v[122:125], v[244:247]
	v_cvt_pk_f16_f32 v152, v212, v213
	v_cvt_pk_f16_f32 v153, v214, v215
	v_mfma_f32_16x16x32_f16 v[176:179], v[54:57], v[126:129], v[244:247]
	v_pk_max_f16 v152, v152, 0
	v_pk_max_f16 v153, v153, 0
	v_mfma_f32_16x16x32_f16 v[180:183], v[54:57], v[134:137], v[244:247]
	v_cvt_pk_f16_f32 v154, v228, v229
	v_cvt_pk_f16_f32 v155, v230, v231
	v_mfma_f32_16x16x32_f16 v[18:21], v[54:57], v[138:141], v[244:247]
	v_pk_max_f16 v154, v154, 0
	v_pk_max_f16 v155, v155, 0
	ds_write_b128 v108, v[152:155] offset:16384
	s_waitcnt vmcnt(17)
	v_mfma_f32_16x16x32_f16 v[54:57], v[50:53], v[122:125], v[248:251]
	v_cvt_pk_f16_f32 v156, v216, v217
	v_cvt_pk_f16_f32 v157, v218, v219
	v_mfma_f32_16x16x32_f16 v[184:187], v[50:53], v[126:129], v[248:251]
	v_pk_max_f16 v156, v156, 0
	v_pk_max_f16 v157, v157, 0
	v_mfma_f32_16x16x32_f16 v[188:191], v[50:53], v[134:137], v[248:251]
	v_cvt_pk_f16_f32 v158, v232, v233
	v_cvt_pk_f16_f32 v159, v234, v235
	v_mfma_f32_16x16x32_f16 v[22:25], v[50:53], v[138:141], v[248:251]
	v_pk_max_f16 v158, v158, 0
	v_pk_max_f16 v159, v159, 0
	ds_write_b128 v108, v[156:159] offset:32768
	s_waitcnt vmcnt(16)
	v_mfma_f32_16x16x32_f16 v[50:53], v[38:41], v[122:125], v[252:255]
	v_cvt_pk_f16_f32 v160, v220, v221
	v_cvt_pk_f16_f32 v161, v222, v223
	v_mfma_f32_16x16x32_f16 v[122:125], v[38:41], v[126:129], v[252:255]
	v_pk_max_f16 v160, v160, 0
	v_pk_max_f16 v161, v161, 0
	v_mfma_f32_16x16x32_f16 v[126:129], v[38:41], v[134:137], v[252:255]
	v_cvt_pk_f16_f32 v162, v236, v237
	v_cvt_pk_f16_f32 v163, v238, v239
	v_mfma_f32_16x16x32_f16 v[38:41], v[38:41], v[138:141], v[252:255]
	v_pk_max_f16 v162, v162, 0
	v_pk_max_f16 v163, v163, 0
	ds_write_b128 v108, v[160:163] offset:49152
	s_add_i32 s9, s22, s35
	s_waitcnt vmcnt(15)
	v_mfma_f32_16x16x32_f16 v[164:167], v[94:97], v[142:145], v[164:167]
	v_mfma_f32_16x16x32_f16 v[168:171], v[94:97], v[152:155], v[168:171]
	s_waitcnt vmcnt(14)
	v_mfma_f32_16x16x32_f16 v[58:61], v[90:93], v[142:145], v[58:61]
	v_mfma_f32_16x16x32_f16 v[176:179], v[90:93], v[152:155], v[176:179]
	s_waitcnt vmcnt(13)
	v_mfma_f32_16x16x32_f16 v[54:57], v[78:81], v[142:145], v[54:57]
	v_mfma_f32_16x16x32_f16 v[184:187], v[78:81], v[152:155], v[184:187]
	s_waitcnt vmcnt(12)
	v_mfma_f32_16x16x32_f16 v[50:53], v[34:37], v[142:145], v[50:53]
	buffer_load_dwordx4 v[140:143], v147, s[16:19], s9 offen
	buffer_load_dwordx4 v[220:223], v148, s[16:19], s9 offen
	v_mfma_f32_16x16x32_f16 v[122:125], v[34:37], v[152:155], v[122:125]
	buffer_load_dwordx4 v[152:155], v149, s[16:19], s9 offen
	buffer_load_dwordx4 v[224:227], v150, s[16:19], s9 offen
	s_mov_b32 s9, s21
	s_waitcnt lgkmcnt(0)
	s_barrier
	v_add_u32_e32 v99, s66, v99
	ds_read_b128 v[136:139], v99
	ds_read_b128 v[208:211], v99 offset:16384
	ds_read_b128 v[212:215], v99 offset:32768
	ds_read_b128 v[216:219], v99 offset:49152
	v_mfma_f32_16x16x32_f16 v[172:175], v[94:97], v[156:159], v[172:175]
	v_mfma_f32_16x16x32_f16 v[94:97], v[94:97], v[160:163], v[10:13]
	s_nop 2
	v_lshl_add_u64 v[10:11], s[8:9], 4, v[130:131]
	v_mfma_f32_16x16x32_f16 v[180:183], v[90:93], v[156:159], v[180:183]
	v_mfma_f32_16x16x32_f16 v[90:93], v[90:93], v[160:163], v[18:21]
	v_mfma_f32_16x16x32_f16 v[188:191], v[78:81], v[156:159], v[188:191]
	v_mfma_f32_16x16x32_f16 v[78:81], v[78:81], v[160:163], v[22:25]
	global_load_dwordx4 v[30:33], v[10:11], off
	s_nop 1
	global_load_dwordx4 v[22:25], v[10:11], off offset:1024
	global_load_dwordx4 v[18:21], v[10:11], off offset:2048
	s_nop 0
	global_load_dwordx4 v[10:13], v[10:11], off offset:3072
	s_nop 0
	global_load_dwordx2 v[134:135], v[0:1], off
	v_mfma_f32_16x16x32_f16 v[126:129], v[34:37], v[156:159], v[126:129]
	v_mfma_f32_16x16x32_f16 v[34:37], v[34:37], v[160:163], v[38:41]
	s_nop 2
	v_add_u32_e32 v100, s67, v100
	ds_read_b128 v[38:41], v100
	ds_read_b128 v[156:159], v100 offset:16384
	ds_read_b128 v[160:163], v100 offset:32768
	ds_read_b128 v[228:231], v100 offset:49152
	s_add_i32 s8, s22, s36
	s_waitcnt vmcnt(20) lgkmcnt(7)
	v_mfma_f32_16x16x32_f16 v[164:167], v[82:85], v[136:139], v[164:167]
	s_waitcnt lgkmcnt(6)
	v_mfma_f32_16x16x32_f16 v[168:171], v[82:85], v[208:211], v[168:171]
	s_waitcnt lgkmcnt(5)
	v_mfma_f32_16x16x32_f16 v[172:175], v[82:85], v[212:215], v[172:175]
	s_waitcnt lgkmcnt(4)
	v_mfma_f32_16x16x32_f16 v[82:85], v[82:85], v[216:219], v[94:97]
	s_waitcnt vmcnt(19)
	v_mfma_f32_16x16x32_f16 v[58:61], v[70:73], v[136:139], v[58:61]
	v_mfma_f32_16x16x32_f16 v[94:97], v[70:73], v[208:211], v[176:179]
	v_mfma_f32_16x16x32_f16 v[176:179], v[70:73], v[212:215], v[180:183]
	v_mfma_f32_16x16x32_f16 v[70:73], v[70:73], v[216:219], v[90:93]
	s_waitcnt vmcnt(18)
	v_mfma_f32_16x16x32_f16 v[54:57], v[62:65], v[136:139], v[54:57]
	v_mfma_f32_16x16x32_f16 v[90:93], v[62:65], v[208:211], v[184:187]
	v_mfma_f32_16x16x32_f16 v[180:183], v[62:65], v[212:215], v[188:191]
	v_mfma_f32_16x16x32_f16 v[62:65], v[62:65], v[216:219], v[78:81]
	s_waitcnt vmcnt(17)
	v_mfma_f32_16x16x32_f16 v[50:53], v[42:45], v[136:139], v[50:53]
	v_mfma_f32_16x16x32_f16 v[78:81], v[42:45], v[208:211], v[122:125]
	v_mfma_f32_16x16x32_f16 v[122:125], v[42:45], v[212:215], v[126:129]
	s_nop 2
	buffer_load_dwordx4 v[126:129], v147, s[16:19], s8 offen
	buffer_load_dwordx4 v[136:139], v148, s[16:19], s8 offen
	buffer_load_dwordx4 v[184:187], v149, s[16:19], s8 offen
	buffer_load_dwordx4 v[188:191], v150, s[16:19], s8 offen
	v_mfma_f32_16x16x32_f16 v[34:37], v[42:45], v[216:219], v[34:37]
	v_add_u32_e32 v111, s68, v111
	ds_read_b128 v[42:45], v111
	ds_read_b128 v[208:211], v111 offset:16384
	ds_read_b128 v[212:215], v111 offset:32768
	ds_read_b128 v[216:219], v111 offset:49152
	s_add_i32 s8, s22, s37
	s_waitcnt vmcnt(20) lgkmcnt(7)
	v_mfma_f32_16x16x32_f16 v[164:167], v[86:89], v[38:41], v[164:167]
	s_waitcnt lgkmcnt(6)
	v_mfma_f32_16x16x32_f16 v[168:171], v[86:89], v[156:159], v[168:171]
	s_waitcnt lgkmcnt(5)
	v_mfma_f32_16x16x32_f16 v[172:175], v[86:89], v[160:163], v[172:175]
	s_waitcnt lgkmcnt(4)
	v_mfma_f32_16x16x32_f16 v[82:85], v[86:89], v[228:231], v[82:85]
	s_waitcnt vmcnt(19)
	v_mfma_f32_16x16x32_f16 v[58:61], v[74:77], v[38:41], v[58:61]
	v_mfma_f32_16x16x32_f16 v[86:89], v[74:77], v[156:159], v[94:97]
	v_mfma_f32_16x16x32_f16 v[94:97], v[74:77], v[160:163], v[176:179]
	v_mfma_f32_16x16x32_f16 v[70:73], v[74:77], v[228:231], v[70:73]
	s_waitcnt vmcnt(18)
	v_mfma_f32_16x16x32_f16 v[54:57], v[66:69], v[38:41], v[54:57]
	v_mfma_f32_16x16x32_f16 v[74:77], v[66:69], v[156:159], v[90:93]
	v_mfma_f32_16x16x32_f16 v[90:93], v[66:69], v[160:163], v[180:183]
	v_mfma_f32_16x16x32_f16 v[62:65], v[66:69], v[228:231], v[62:65]
	s_waitcnt vmcnt(17)
	v_mfma_f32_16x16x32_f16 v[38:41], v[46:49], v[38:41], v[50:53]
	v_mfma_f32_16x16x32_f16 v[50:53], v[46:49], v[156:159], v[78:81]
	v_mfma_f32_16x16x32_f16 v[66:69], v[46:49], v[160:163], v[122:125]
	s_nop 1
	buffer_load_dwordx4 v[78:81], v147, s[16:19], s8 offen
	buffer_load_dwordx4 v[122:125], v148, s[16:19], s8 offen
	buffer_load_dwordx4 v[156:159], v149, s[16:19], s8 offen
	buffer_load_dwordx4 v[160:163], v150, s[16:19], s8 offen
	v_mfma_f32_16x16x32_f16 v[34:37], v[46:49], v[228:231], v[34:37]
	v_add_u32_e32 v98, s69, v98
	ds_read_b128 v[46:49], v98
	ds_read_b128 v[176:179], v98 offset:16384
	ds_read_b128 v[180:183], v98 offset:32768
	ds_read_b128 v[228:231], v98 offset:49152
	s_add_i32 s8, s22, s38
	s_waitcnt vmcnt(20) lgkmcnt(7)
	v_mfma_f32_16x16x32_f16 v[164:167], v[192:195], v[42:45], v[164:167]
	s_waitcnt lgkmcnt(6)
	v_mfma_f32_16x16x32_f16 v[168:171], v[192:195], v[208:211], v[168:171]
	s_waitcnt lgkmcnt(5)
	v_mfma_f32_16x16x32_f16 v[172:175], v[192:195], v[212:215], v[172:175]
	s_waitcnt lgkmcnt(4)
	v_mfma_f32_16x16x32_f16 v[82:85], v[192:195], v[216:219], v[82:85]
	s_waitcnt vmcnt(19)
	v_mfma_f32_16x16x32_f16 v[58:61], v[196:199], v[42:45], v[58:61]
	v_mfma_f32_16x16x32_f16 v[86:89], v[196:199], v[208:211], v[86:89]
	v_mfma_f32_16x16x32_f16 v[94:97], v[196:199], v[212:215], v[94:97]
	v_mfma_f32_16x16x32_f16 v[70:73], v[196:199], v[216:219], v[70:73]
	s_waitcnt vmcnt(18)
	v_mfma_f32_16x16x32_f16 v[54:57], v[200:203], v[42:45], v[54:57]
	v_mfma_f32_16x16x32_f16 v[74:77], v[200:203], v[208:211], v[74:77]
	v_mfma_f32_16x16x32_f16 v[90:93], v[200:203], v[212:215], v[90:93]
	v_mfma_f32_16x16x32_f16 v[62:65], v[200:203], v[216:219], v[62:65]
	s_waitcnt vmcnt(17)
	v_mfma_f32_16x16x32_f16 v[38:41], v[204:207], v[42:45], v[38:41]
	v_mfma_f32_16x16x32_f16 v[42:45], v[204:207], v[208:211], v[50:53]
	v_mfma_f32_16x16x32_f16 v[50:53], v[204:207], v[212:215], v[66:69]
	s_nop 2
	buffer_load_dwordx4 v[66:69], v147, s[16:19], s8 offen
	buffer_load_dwordx4 v[192:195], v148, s[16:19], s8 offen
	buffer_load_dwordx4 v[196:199], v149, s[16:19], s8 offen
	buffer_load_dwordx4 v[200:203], v150, s[16:19], s8 offen
	v_mfma_f32_16x16x32_f16 v[34:37], v[204:207], v[216:219], v[34:37]
	v_add_u32_e32 v99, s70, v99
	ds_read_b128 v[204:207], v99
	ds_read_b128 v[208:211], v99 offset:16384
	ds_read_b128 v[212:215], v99 offset:32768
	ds_read_b128 v[216:219], v99 offset:49152
	s_add_i32 s8, s22, s39
	s_waitcnt vmcnt(20) lgkmcnt(7)
	v_mfma_f32_16x16x32_f16 v[164:167], v[140:143], v[46:49], v[164:167]
	s_waitcnt lgkmcnt(6)
	v_mfma_f32_16x16x32_f16 v[168:171], v[140:143], v[176:179], v[168:171]
	s_waitcnt lgkmcnt(5)
	v_mfma_f32_16x16x32_f16 v[172:175], v[140:143], v[180:183], v[172:175]
	s_waitcnt lgkmcnt(4)
	v_mfma_f32_16x16x32_f16 v[82:85], v[140:143], v[228:231], v[82:85]
	s_waitcnt vmcnt(19)
	v_mfma_f32_16x16x32_f16 v[58:61], v[220:223], v[46:49], v[58:61]
	v_mfma_f32_16x16x32_f16 v[86:89], v[220:223], v[176:179], v[86:89]
	s_waitcnt vmcnt(18)
	v_mfma_f32_16x16x32_f16 v[54:57], v[152:155], v[46:49], v[54:57]
	v_mfma_f32_16x16x32_f16 v[74:77], v[152:155], v[176:179], v[74:77]
	v_mfma_f32_16x16x32_f16 v[90:93], v[152:155], v[180:183], v[90:93]
	v_mfma_f32_16x16x32_f16 v[62:65], v[152:155], v[228:231], v[62:65]
	s_waitcnt vmcnt(17)
	v_mfma_f32_16x16x32_f16 v[38:41], v[224:227], v[46:49], v[38:41]
	v_mfma_f32_16x16x32_f16 v[42:45], v[224:227], v[176:179], v[42:45]
	v_mfma_f32_16x16x32_f16 v[46:49], v[224:227], v[180:183], v[50:53]
	s_nop 2
	buffer_load_dwordx4 v[50:53], v147, s[16:19], s8 offen
	buffer_load_dwordx4 v[140:143], v148, s[16:19], s8 offen
	buffer_load_dwordx4 v[152:155], v149, s[16:19], s8 offen
	buffer_load_dwordx4 v[176:179], v150, s[16:19], s8 offen
	v_mfma_f32_16x16x32_f16 v[94:97], v[220:223], v[180:183], v[94:97]
	v_mfma_f32_16x16x32_f16 v[70:73], v[220:223], v[228:231], v[70:73]
	v_mfma_f32_16x16x32_f16 v[34:37], v[224:227], v[228:231], v[34:37]
	v_add_u32_e32 v100, s71, v100
	ds_read_b128 v[180:183], v100
	ds_read_b128 v[220:223], v100 offset:16384
	ds_read_b128 v[224:227], v100 offset:32768
	ds_read_b128 v[228:231], v100 offset:49152
	s_add_i32 s8, s22, s40
	s_waitcnt vmcnt(15) lgkmcnt(7)
	v_mfma_f32_16x16x32_f16 v[164:167], v[126:129], v[204:207], v[164:167]
	s_waitcnt lgkmcnt(6)
	v_mfma_f32_16x16x32_f16 v[168:171], v[126:129], v[208:211], v[168:171]
	s_waitcnt lgkmcnt(5)
	v_mfma_f32_16x16x32_f16 v[172:175], v[126:129], v[212:215], v[172:175]
	s_waitcnt lgkmcnt(4)
	v_mfma_f32_16x16x32_f16 v[82:85], v[126:129], v[216:219], v[82:85]
	s_waitcnt vmcnt(14)
	v_mfma_f32_16x16x32_f16 v[58:61], v[136:139], v[204:207], v[58:61]
	v_mfma_f32_16x16x32_f16 v[86:89], v[136:139], v[208:211], v[86:89]
	v_mfma_f32_16x16x32_f16 v[94:97], v[136:139], v[212:215], v[94:97]
	v_mfma_f32_16x16x32_f16 v[70:73], v[136:139], v[216:219], v[70:73]
	s_waitcnt vmcnt(13)
	v_mfma_f32_16x16x32_f16 v[54:57], v[184:187], v[204:207], v[54:57]
	v_mfma_f32_16x16x32_f16 v[74:77], v[184:187], v[208:211], v[74:77]
	v_mfma_f32_16x16x32_f16 v[90:93], v[184:187], v[212:215], v[90:93]
	v_mfma_f32_16x16x32_f16 v[62:65], v[184:187], v[216:219], v[62:65]
	s_waitcnt vmcnt(12)
	v_mfma_f32_16x16x32_f16 v[38:41], v[188:191], v[204:207], v[38:41]
	buffer_load_dwordx4 v[126:129], v147, s[16:19], s8 offen
	buffer_load_dwordx4 v[136:139], v148, s[16:19], s8 offen
	buffer_load_dwordx4 v[184:187], v149, s[16:19], s8 offen
	buffer_load_dwordx4 v[204:207], v150, s[16:19], s8 offen
	v_mfma_f32_16x16x32_f16 v[42:45], v[188:191], v[208:211], v[42:45]
	v_mfma_f32_16x16x32_f16 v[46:49], v[188:191], v[212:215], v[46:49]
	v_mfma_f32_16x16x32_f16 v[34:37], v[188:191], v[216:219], v[34:37]
	v_add_u32_e32 v111, s72, v111
	ds_read_b128 v[188:191], v111
	ds_read_b128 v[208:211], v111 offset:16384
	ds_read_b128 v[212:215], v111 offset:32768
	ds_read_b128 v[216:219], v111 offset:49152
	s_add_i32 s8, s22, s41
	s_waitcnt vmcnt(15) lgkmcnt(7)
	v_mfma_f32_16x16x32_f16 v[164:167], v[78:81], v[180:183], v[164:167]
	s_waitcnt lgkmcnt(6)
	v_mfma_f32_16x16x32_f16 v[168:171], v[78:81], v[220:223], v[168:171]
	s_waitcnt lgkmcnt(5)
	v_mfma_f32_16x16x32_f16 v[172:175], v[78:81], v[224:227], v[172:175]
	s_waitcnt lgkmcnt(4)
	v_mfma_f32_16x16x32_f16 v[78:81], v[78:81], v[228:231], v[82:85]
	s_waitcnt vmcnt(14)
	v_mfma_f32_16x16x32_f16 v[58:61], v[122:125], v[180:183], v[58:61]
	v_mfma_f32_16x16x32_f16 v[82:85], v[122:125], v[220:223], v[86:89]
	v_mfma_f32_16x16x32_f16 v[86:89], v[122:125], v[224:227], v[94:97]
	v_mfma_f32_16x16x32_f16 v[70:73], v[122:125], v[228:231], v[70:73]
	s_waitcnt vmcnt(13)
	v_mfma_f32_16x16x32_f16 v[54:57], v[156:159], v[180:183], v[54:57]
	v_mfma_f32_16x16x32_f16 v[74:77], v[156:159], v[220:223], v[74:77]
	v_mfma_f32_16x16x32_f16 v[90:93], v[156:159], v[224:227], v[90:93]
	v_mfma_f32_16x16x32_f16 v[62:65], v[156:159], v[228:231], v[62:65]
	s_waitcnt vmcnt(12)
	v_mfma_f32_16x16x32_f16 v[38:41], v[160:163], v[180:183], v[38:41]
	buffer_load_dwordx4 v[94:97], v147, s[16:19], s8 offen
	buffer_load_dwordx4 v[122:125], v148, s[16:19], s8 offen
	buffer_load_dwordx4 v[156:159], v149, s[16:19], s8 offen
	buffer_load_dwordx4 v[180:183], v150, s[16:19], s8 offen
	v_mfma_f32_16x16x32_f16 v[42:45], v[160:163], v[220:223], v[42:45]
	v_mfma_f32_16x16x32_f16 v[46:49], v[160:163], v[224:227], v[46:49]
	v_mfma_f32_16x16x32_f16 v[34:37], v[160:163], v[228:231], v[34:37]
	v_add_u32_e32 v98, s73, v98
	ds_read_b128 v[160:163], v98
	ds_read_b128 v[220:223], v98 offset:16384
	ds_read_b128 v[224:227], v98 offset:32768
	ds_read_b128 v[228:231], v98 offset:49152
	s_add_i32 s8, s22, s42
	s_waitcnt vmcnt(15) lgkmcnt(7)
	v_mfma_f32_16x16x32_f16 v[164:167], v[66:69], v[188:191], v[164:167]
	s_waitcnt lgkmcnt(6)
	v_mfma_f32_16x16x32_f16 v[168:171], v[66:69], v[208:211], v[168:171]
	s_waitcnt lgkmcnt(5)
	v_mfma_f32_16x16x32_f16 v[172:175], v[66:69], v[212:215], v[172:175]
	s_waitcnt lgkmcnt(4)
	v_mfma_f32_16x16x32_f16 v[66:69], v[66:69], v[216:219], v[78:81]
	s_waitcnt vmcnt(14)
	v_mfma_f32_16x16x32_f16 v[58:61], v[192:195], v[188:191], v[58:61]
	v_mfma_f32_16x16x32_f16 v[78:81], v[192:195], v[208:211], v[82:85]
	v_mfma_f32_16x16x32_f16 v[82:85], v[192:195], v[212:215], v[86:89]
	v_mfma_f32_16x16x32_f16 v[70:73], v[192:195], v[216:219], v[70:73]
	s_waitcnt vmcnt(13)
	v_mfma_f32_16x16x32_f16 v[54:57], v[196:199], v[188:191], v[54:57]
	v_mfma_f32_16x16x32_f16 v[74:77], v[196:199], v[208:211], v[74:77]
	v_mfma_f32_16x16x32_f16 v[86:89], v[196:199], v[212:215], v[90:93]
	v_mfma_f32_16x16x32_f16 v[62:65], v[196:199], v[216:219], v[62:65]
	s_waitcnt vmcnt(12)
	v_mfma_f32_16x16x32_f16 v[38:41], v[200:203], v[188:191], v[38:41]
	buffer_load_dwordx4 v[90:93], v147, s[16:19], s8 offen
	buffer_load_dwordx4 v[188:191], v148, s[16:19], s8 offen
	buffer_load_dwordx4 v[192:195], v149, s[16:19], s8 offen
	buffer_load_dwordx4 v[196:199], v150, s[16:19], s8 offen
	v_mfma_f32_16x16x32_f16 v[42:45], v[200:203], v[208:211], v[42:45]
	v_mfma_f32_16x16x32_f16 v[46:49], v[200:203], v[212:215], v[46:49]
	v_mfma_f32_16x16x32_f16 v[34:37], v[200:203], v[216:219], v[34:37]
	v_add_u32_e32 v99, s74, v99
	ds_read_b128 v[200:203], v99
	ds_read_b128 v[208:211], v99 offset:16384
	ds_read_b128 v[212:215], v99 offset:32768
	ds_read_b128 v[216:219], v99 offset:49152
	s_add_i32 s8, s22, s43
	s_waitcnt vmcnt(15) lgkmcnt(7)
	v_mfma_f32_16x16x32_f16 v[164:167], v[50:53], v[160:163], v[164:167]
	s_waitcnt lgkmcnt(6)
	v_mfma_f32_16x16x32_f16 v[168:171], v[50:53], v[220:223], v[168:171]
	s_waitcnt lgkmcnt(5)
	v_mfma_f32_16x16x32_f16 v[172:175], v[50:53], v[224:227], v[172:175]
	s_waitcnt lgkmcnt(4)
	v_mfma_f32_16x16x32_f16 v[50:53], v[50:53], v[228:231], v[66:69]
	s_waitcnt vmcnt(14)
	v_mfma_f32_16x16x32_f16 v[58:61], v[140:143], v[160:163], v[58:61]
	v_mfma_f32_16x16x32_f16 v[66:69], v[140:143], v[220:223], v[78:81]
	v_mfma_f32_16x16x32_f16 v[78:81], v[140:143], v[224:227], v[82:85]
	v_mfma_f32_16x16x32_f16 v[70:73], v[140:143], v[228:231], v[70:73]
	s_waitcnt vmcnt(13)
	v_mfma_f32_16x16x32_f16 v[54:57], v[152:155], v[160:163], v[54:57]
	v_mfma_f32_16x16x32_f16 v[74:77], v[152:155], v[220:223], v[74:77]
	v_mfma_f32_16x16x32_f16 v[82:85], v[152:155], v[224:227], v[86:89]
	v_mfma_f32_16x16x32_f16 v[62:65], v[152:155], v[228:231], v[62:65]
	s_waitcnt vmcnt(12)
	v_mfma_f32_16x16x32_f16 v[38:41], v[176:179], v[160:163], v[38:41]
	buffer_load_dwordx4 v[86:89], v147, s[16:19], s8 offen
	buffer_load_dwordx4 v[140:143], v148, s[16:19], s8 offen
	buffer_load_dwordx4 v[152:155], v149, s[16:19], s8 offen
	buffer_load_dwordx4 v[160:163], v150, s[16:19], s8 offen
	v_mfma_f32_16x16x32_f16 v[42:45], v[176:179], v[220:223], v[42:45]
	v_mfma_f32_16x16x32_f16 v[46:49], v[176:179], v[224:227], v[46:49]
	v_mfma_f32_16x16x32_f16 v[34:37], v[176:179], v[228:231], v[34:37]
	v_add_u32_e32 v100, s75, v100
	ds_read_b128 v[176:179], v100
	ds_read_b128 v[220:223], v100 offset:16384
	ds_read_b128 v[224:227], v100 offset:32768
	ds_read_b128 v[228:231], v100 offset:49152
	s_add_i32 s8, s22, s44
	s_waitcnt vmcnt(15) lgkmcnt(7)
	v_mfma_f32_16x16x32_f16 v[164:167], v[126:129], v[200:203], v[164:167]
	s_waitcnt lgkmcnt(6)
	v_mfma_f32_16x16x32_f16 v[168:171], v[126:129], v[208:211], v[168:171]
	s_waitcnt lgkmcnt(5)
	v_mfma_f32_16x16x32_f16 v[172:175], v[126:129], v[212:215], v[172:175]
	s_waitcnt lgkmcnt(4)
	v_mfma_f32_16x16x32_f16 v[50:53], v[126:129], v[216:219], v[50:53]
	s_waitcnt vmcnt(14)
	v_mfma_f32_16x16x32_f16 v[58:61], v[136:139], v[200:203], v[58:61]
	v_mfma_f32_16x16x32_f16 v[66:69], v[136:139], v[208:211], v[66:69]
	v_mfma_f32_16x16x32_f16 v[78:81], v[136:139], v[212:215], v[78:81]
	v_mfma_f32_16x16x32_f16 v[70:73], v[136:139], v[216:219], v[70:73]
	s_waitcnt vmcnt(13)
	v_mfma_f32_16x16x32_f16 v[54:57], v[184:187], v[200:203], v[54:57]
	v_mfma_f32_16x16x32_f16 v[74:77], v[184:187], v[208:211], v[74:77]
	v_mfma_f32_16x16x32_f16 v[82:85], v[184:187], v[212:215], v[82:85]
	v_mfma_f32_16x16x32_f16 v[62:65], v[184:187], v[216:219], v[62:65]
	s_waitcnt vmcnt(12)
	v_mfma_f32_16x16x32_f16 v[38:41], v[204:207], v[200:203], v[38:41]
	buffer_load_dwordx4 v[126:129], v147, s[16:19], s8 offen
	buffer_load_dwordx4 v[136:139], v148, s[16:19], s8 offen
	buffer_load_dwordx4 v[184:187], v149, s[16:19], s8 offen
	buffer_load_dwordx4 v[200:203], v150, s[16:19], s8 offen
	v_mfma_f32_16x16x32_f16 v[42:45], v[204:207], v[208:211], v[42:45]
	v_mfma_f32_16x16x32_f16 v[46:49], v[204:207], v[212:215], v[46:49]
	v_mfma_f32_16x16x32_f16 v[34:37], v[204:207], v[216:219], v[34:37]
	v_add_u32_e32 v111, s76, v111
	ds_read_b128 v[204:207], v111
	ds_read_b128 v[208:211], v111 offset:16384
	ds_read_b128 v[212:215], v111 offset:32768
	ds_read_b128 v[216:219], v111 offset:49152
	s_add_i32 s8, s22, s45
	s_waitcnt vmcnt(15) lgkmcnt(7)
	v_mfma_f32_16x16x32_f16 v[164:167], v[94:97], v[176:179], v[164:167]
	s_waitcnt lgkmcnt(6)
	v_mfma_f32_16x16x32_f16 v[168:171], v[94:97], v[220:223], v[168:171]
	s_waitcnt vmcnt(14)
	v_mfma_f32_16x16x32_f16 v[58:61], v[122:125], v[176:179], v[58:61]
	v_mfma_f32_16x16x32_f16 v[66:69], v[122:125], v[220:223], v[66:69]
	s_waitcnt lgkmcnt(5)
	v_mfma_f32_16x16x32_f16 v[78:81], v[122:125], v[224:227], v[78:81]
	s_waitcnt lgkmcnt(4)
	v_mfma_f32_16x16x32_f16 v[70:73], v[122:125], v[228:231], v[70:73]
	s_waitcnt vmcnt(13)
	v_mfma_f32_16x16x32_f16 v[54:57], v[156:159], v[176:179], v[54:57]
	v_mfma_f32_16x16x32_f16 v[74:77], v[156:159], v[220:223], v[74:77]
	v_mfma_f32_16x16x32_f16 v[82:85], v[156:159], v[224:227], v[82:85]
	v_mfma_f32_16x16x32_f16 v[62:65], v[156:159], v[228:231], v[62:65]
	s_waitcnt vmcnt(12)
	v_mfma_f32_16x16x32_f16 v[38:41], v[180:183], v[176:179], v[38:41]
	v_mfma_f32_16x16x32_f16 v[42:45], v[180:183], v[220:223], v[42:45]
	buffer_load_dwordx4 v[122:125], v147, s[16:19], s8 offen
	buffer_load_dwordx4 v[156:159], v148, s[16:19], s8 offen
	buffer_load_dwordx4 v[176:179], v149, s[16:19], s8 offen
	buffer_load_dwordx4 v[220:223], v150, s[16:19], s8 offen
	v_mfma_f32_16x16x32_f16 v[50:53], v[94:97], v[228:231], v[50:53]
	v_mfma_f32_16x16x32_f16 v[46:49], v[180:183], v[224:227], v[46:49]
	v_mfma_f32_16x16x32_f16 v[34:37], v[180:183], v[228:231], v[34:37]
	v_mfma_f32_16x16x32_f16 v[172:175], v[94:97], v[224:227], v[172:175]
	v_add_u32_e32 v98, s77, v98
	ds_read_b128 v[94:97], v98
	ds_read_b128 v[180:183], v98 offset:16384
	ds_read_b128 v[224:227], v98 offset:32768
	ds_read_b128 v[228:231], v98 offset:49152
	s_add_i32 s8, s22, s46
	s_waitcnt vmcnt(15) lgkmcnt(7)
	v_mfma_f32_16x16x32_f16 v[164:167], v[90:93], v[204:207], v[164:167]
	s_waitcnt lgkmcnt(6)
	v_mfma_f32_16x16x32_f16 v[168:171], v[90:93], v[208:211], v[168:171]
	s_waitcnt lgkmcnt(5)
	v_mfma_f32_16x16x32_f16 v[172:175], v[90:93], v[212:215], v[172:175]
	s_waitcnt lgkmcnt(4)
	v_mfma_f32_16x16x32_f16 v[90:93], v[90:93], v[216:219], v[50:53]
	s_waitcnt vmcnt(14)
	v_mfma_f32_16x16x32_f16 v[232:235], v[188:191], v[204:207], v[58:61]
	v_mfma_f32_16x16x32_f16 v[66:69], v[188:191], v[208:211], v[66:69]
	v_mfma_f32_16x16x32_f16 v[78:81], v[188:191], v[212:215], v[78:81]
	v_mfma_f32_16x16x32_f16 v[70:73], v[188:191], v[216:219], v[70:73]
	s_waitcnt vmcnt(13)
	v_mfma_f32_16x16x32_f16 v[188:191], v[192:195], v[204:207], v[54:57]
	v_mfma_f32_16x16x32_f16 v[74:77], v[192:195], v[208:211], v[74:77]
	v_mfma_f32_16x16x32_f16 v[82:85], v[192:195], v[212:215], v[82:85]
	v_mfma_f32_16x16x32_f16 v[62:65], v[192:195], v[216:219], v[62:65]
	s_waitcnt vmcnt(12)
	v_mfma_f32_16x16x32_f16 v[192:195], v[196:199], v[204:207], v[38:41]
	buffer_load_dwordx4 v[58:61], v147, s[16:19], s8 offen
	buffer_load_dwordx4 v[54:57], v148, s[16:19], s8 offen
	buffer_load_dwordx4 v[50:53], v149, s[16:19], s8 offen
	buffer_load_dwordx4 v[38:41], v150, s[16:19], s8 offen
	v_mfma_f32_16x16x32_f16 v[42:45], v[196:199], v[208:211], v[42:45]
	v_mfma_f32_16x16x32_f16 v[46:49], v[196:199], v[212:215], v[46:49]
	v_mfma_f32_16x16x32_f16 v[196:199], v[196:199], v[216:219], v[34:37]
	v_add_u32_e32 v99, s78, v99
	ds_read_b128 v[204:207], v99
	ds_read_b128 v[208:211], v99 offset:16384
	ds_read_b128 v[212:215], v99 offset:32768
	ds_read_b128 v[216:219], v99 offset:49152
	s_add_i32 s8, s22, s47
	s_waitcnt vmcnt(15) lgkmcnt(7)
	v_mfma_f32_16x16x32_f16 v[164:167], v[86:89], v[94:97], v[164:167]
	s_waitcnt lgkmcnt(6)
	v_mfma_f32_16x16x32_f16 v[168:171], v[86:89], v[180:183], v[168:171]
	s_waitcnt lgkmcnt(5)
	v_mfma_f32_16x16x32_f16 v[172:175], v[86:89], v[224:227], v[172:175]
	s_waitcnt lgkmcnt(4)
	v_mfma_f32_16x16x32_f16 v[86:89], v[86:89], v[228:231], v[90:93]
	s_waitcnt vmcnt(14)
	v_mfma_f32_16x16x32_f16 v[232:235], v[140:143], v[94:97], v[232:235]
	v_mfma_f32_16x16x32_f16 v[66:69], v[140:143], v[180:183], v[66:69]
	v_mfma_f32_16x16x32_f16 v[236:239], v[140:143], v[224:227], v[78:81]
	v_mfma_f32_16x16x32_f16 v[70:73], v[140:143], v[228:231], v[70:73]
	s_waitcnt vmcnt(13)
	v_mfma_f32_16x16x32_f16 v[140:143], v[152:155], v[94:97], v[188:191]
	v_mfma_f32_16x16x32_f16 v[74:77], v[152:155], v[180:183], v[74:77]
	v_mfma_f32_16x16x32_f16 v[82:85], v[152:155], v[224:227], v[82:85]
	v_mfma_f32_16x16x32_f16 v[62:65], v[152:155], v[228:231], v[62:65]
	s_waitcnt vmcnt(12)
	v_mfma_f32_16x16x32_f16 v[152:155], v[160:163], v[94:97], v[192:195]
	buffer_load_dwordx4 v[94:97], v147, s[16:19], s8 offen
	buffer_load_dwordx4 v[90:93], v148, s[16:19], s8 offen
	buffer_load_dwordx4 v[78:81], v149, s[16:19], s8 offen
	buffer_load_dwordx4 v[34:37], v150, s[16:19], s8 offen
	v_mfma_f32_16x16x32_f16 v[42:45], v[160:163], v[180:183], v[42:45]
	v_mfma_f32_16x16x32_f16 v[46:49], v[160:163], v[224:227], v[46:49]
	v_mfma_f32_16x16x32_f16 v[160:163], v[160:163], v[228:231], v[196:199]
	v_add_u32_e32 v100, s79, v100
	ds_read_b128 v[180:183], v100
	ds_read_b128 v[188:191], v100 offset:16384
	ds_read_b128 v[192:195], v100 offset:32768
	ds_read_b128 v[196:199], v100 offset:49152
	s_add_i32 s8, s22, s48
	s_waitcnt vmcnt(15) lgkmcnt(7)
	v_mfma_f32_16x16x32_f16 v[164:167], v[126:129], v[204:207], v[164:167]
	s_waitcnt lgkmcnt(6)
	v_mfma_f32_16x16x32_f16 v[168:171], v[126:129], v[208:211], v[168:171]
	s_waitcnt lgkmcnt(5)
	v_mfma_f32_16x16x32_f16 v[172:175], v[126:129], v[212:215], v[172:175]
	s_waitcnt lgkmcnt(4)
	v_mfma_f32_16x16x32_f16 v[86:89], v[126:129], v[216:219], v[86:89]
	s_waitcnt vmcnt(14)
	v_mfma_f32_16x16x32_f16 v[126:129], v[136:139], v[204:207], v[232:235]
	v_mfma_f32_16x16x32_f16 v[66:69], v[136:139], v[208:211], v[66:69]
	v_mfma_f32_16x16x32_f16 v[224:227], v[136:139], v[212:215], v[236:239]
	v_mfma_f32_16x16x32_f16 v[136:139], v[136:139], v[216:219], v[70:73]
	s_waitcnt vmcnt(13)
	v_mfma_f32_16x16x32_f16 v[140:143], v[184:187], v[204:207], v[140:143]
	v_mfma_f32_16x16x32_f16 v[74:77], v[184:187], v[208:211], v[74:77]
	v_mfma_f32_16x16x32_f16 v[228:231], v[184:187], v[212:215], v[82:85]
	v_mfma_f32_16x16x32_f16 v[184:187], v[184:187], v[216:219], v[62:65]
	s_waitcnt vmcnt(12)
	v_mfma_f32_16x16x32_f16 v[152:155], v[200:203], v[204:207], v[152:155]
	v_mfma_f32_16x16x32_f16 v[204:207], v[200:203], v[208:211], v[42:45]
	buffer_load_dwordx4 v[82:85], v147, s[16:19], s8 offen
	buffer_load_dwordx4 v[70:73], v148, s[16:19], s8 offen
	buffer_load_dwordx4 v[62:65], v149, s[16:19], s8 offen
	buffer_load_dwordx4 v[42:45], v150, s[16:19], s8 offen
	v_mfma_f32_16x16x32_f16 v[46:49], v[200:203], v[212:215], v[46:49]
	v_mfma_f32_16x16x32_f16 v[160:163], v[200:203], v[216:219], v[160:163]
	v_add_u32_e32 v0, 0x1ac00, v104
	ds_read_b128 v[240:243], v0
	ds_read_b128 v[244:247], v0 offset:16
	s_waitcnt vmcnt(12) lgkmcnt(5)
	v_mfma_f32_16x16x32_f16 v[164:167], v[122:125], v[180:183], v[164:167]
	v_mfma_f32_16x16x32_f16 v[126:129], v[156:159], v[180:183], v[126:129]
	v_mfma_f32_16x16x32_f16 v[140:143], v[176:179], v[180:183], v[140:143]
	v_mfma_f32_16x16x32_f16 v[152:155], v[220:223], v[180:183], v[152:155]
	s_waitcnt lgkmcnt(4)
	v_mfma_f32_16x16x32_f16 v[168:171], v[122:125], v[188:191], v[168:171]
	v_mfma_f32_16x16x32_f16 v[208:211], v[156:159], v[188:191], v[66:69]
	v_mfma_f32_16x16x32_f16 v[212:215], v[176:179], v[188:191], v[74:77]
	v_mfma_f32_16x16x32_f16 v[204:207], v[220:223], v[188:191], v[204:207]
	s_waitcnt lgkmcnt(3)
	v_mfma_f32_16x16x32_f16 v[172:175], v[122:125], v[192:195], v[172:175]
	v_cvt_pk_f16_f32 v232, v164, v165
	v_cvt_pk_f16_f32 v233, v166, v167
	v_pk_max_f16 v232, v232, 0
	v_pk_max_f16 v233, v233, 0
	v_mfma_f32_16x16x32_f16 v[224:227], v[156:159], v[192:195], v[224:227]
	v_cvt_pk_f16_f32 v234, v126, v127
	v_cvt_pk_f16_f32 v235, v128, v129
	v_pk_max_f16 v234, v234, 0
	v_pk_max_f16 v235, v235, 0
	v_mfma_f32_16x16x32_f16 v[228:231], v[176:179], v[192:195], v[228:231]
	v_cvt_pk_f16_f32 v236, v140, v141
	v_cvt_pk_f16_f32 v237, v142, v143
	v_pk_max_f16 v236, v236, 0
	v_pk_max_f16 v237, v237, 0
	v_mfma_f32_16x16x32_f16 v[216:219], v[220:223], v[192:195], v[46:49]
	v_cvt_pk_f16_f32 v238, v152, v153
	v_cvt_pk_f16_f32 v239, v154, v155
	v_pk_max_f16 v238, v238, 0
	v_pk_max_f16 v239, v239, 0
	s_waitcnt lgkmcnt(2)
	v_mfma_f32_16x16x32_f16 v[200:203], v[122:125], v[196:199], v[86:89]
	v_cvt_pk_f16_f32 v180, v168, v169
	v_cvt_pk_f16_f32 v181, v170, v171
	v_pk_max_f16 v180, v180, 0
	v_pk_max_f16 v181, v181, 0
	s_add_i32 s8, s22, s49
	buffer_load_dwordx4 v[86:89], v147, s[16:19], s8 offen
	buffer_load_dwordx4 v[74:77], v148, s[16:19], s8 offen
	buffer_load_dwordx4 v[66:69], v149, s[16:19], s8 offen
	buffer_load_dwordx4 v[46:49], v150, s[16:19], s8 offen
	v_mfma_f32_16x16x32_f16 v[136:139], v[156:159], v[196:199], v[136:139]
	v_cvt_pk_f16_f32 v182, v208, v209
	v_cvt_pk_f16_f32 v183, v210, v211
	v_pk_max_f16 v182, v182, 0
	v_pk_max_f16 v183, v183, 0
	s_waitcnt lgkmcnt(1)
	v_mfma_f32_16x16x32_f16 v[252:255], v[240:243], v[232:235], 0
	v_cvt_pk_f16_f32 v232, v172, v173
	v_cvt_pk_f16_f32 v233, v174, v175
	v_pk_max_f16 v232, v232, 0
	v_pk_max_f16 v233, v233, 0
	v_mfma_f32_16x16x32_f16 v[184:187], v[176:179], v[196:199], v[184:187]
	v_cvt_pk_f16_f32 v188, v212, v213
	v_cvt_pk_f16_f32 v189, v214, v215
	v_pk_max_f16 v188, v188, 0
	v_pk_max_f16 v189, v189, 0
	s_waitcnt lgkmcnt(0)
	v_mfma_f32_16x16x32_f16 v[252:255], v[244:247], v[236:239], v[252:255]
	ds_read_u16 v102, v114
	ds_read_u16 v103, v114 offset:512
	ds_read_u16 v115, v114 offset:1024
	ds_read_u16 v116, v114 offset:1536
	v_cvt_pk_f16_f32 v234, v224, v225
	v_cvt_pk_f16_f32 v235, v226, v227
	v_pk_max_f16 v234, v234, 0
	v_pk_max_f16 v235, v235, 0
	v_mfma_f32_16x16x32_f16 v[160:163], v[220:223], v[196:199], v[160:163]
	v_cvt_pk_f16_f32 v190, v204, v205
	v_cvt_pk_f16_f32 v191, v206, v207
	v_pk_max_f16 v190, v190, 0
	v_pk_max_f16 v191, v191, 0
	v_mfma_f32_16x16x32_f16 v[192:195], v[240:243], v[180:183], 0
	v_cvt_pk_f16_f32 v236, v228, v229
	v_cvt_pk_f16_f32 v237, v230, v231
	v_pk_max_f16 v236, v236, 0
	v_pk_max_f16 v237, v237, 0
	v_mfma_f32_16x16x32_f16 v[192:195], v[244:247], v[188:191], v[192:195]
	v_cvt_pk_f16_f32 v238, v216, v217
	v_cvt_pk_f16_f32 v239, v218, v219
	v_pk_max_f16 v238, v238, 0
	v_pk_max_f16 v239, v239, 0
	v_cvt_pk_f16_f32 v180, v200, v201
	v_cvt_pk_f16_f32 v181, v202, v203
	v_pk_max_f16 v180, v180, 0
	v_pk_max_f16 v181, v181, 0
	v_mfma_f32_16x16x32_f16 v[196:199], v[240:243], v[232:235], 0
	v_cvt_pk_f16_f32 v182, v136, v137
	v_cvt_pk_f16_f32 v183, v138, v139
	v_pk_max_f16 v182, v182, 0
	v_pk_max_f16 v183, v183, 0
	v_mfma_f32_16x16x32_f16 v[196:199], v[244:247], v[236:239], v[196:199]
	v_cvt_pk_f16_f32 v188, v184, v185
	v_cvt_pk_f16_f32 v189, v186, v187
	v_pk_max_f16 v188, v188, 0
	v_pk_max_f16 v189, v189, 0
	v_cvt_pk_f16_f32 v190, v160, v161
	v_cvt_pk_f16_f32 v191, v162, v163
	v_pk_max_f16 v190, v190, 0
	v_pk_max_f16 v191, v191, 0
	v_mfma_f32_16x16x32_f16 v[122:125], v[240:243], v[180:183], 0
	s_nop 0
	v_mfma_f32_16x16x32_f16 v[122:125], v[244:247], v[188:191], v[122:125]
	v_add_u32_e32 v145, 0x12c00, v105
	v_cndmask_b32_e64 v0, v252, v192, s[2:3]
	v_cndmask_b32_e64 v0, v0, v196, s[0:1]
	s_waitcnt vmcnt(16)
	v_cndmask_b32_e64 v1, v30, v134, s[0:1]
	v_bfi_b32 v30, s10, v1, v30
	v_perm_b32 v1, v22, v134, s24
	v_cndmask_b32_e64 v22, v22, v1, s[0:1]
	v_cndmask_b32_e64 v0, v0, v122, s[26:27]
	ds_write_b32 v112, v0
	ds_read_b128 v[240:243], v145 offset:2048
	ds_read_b128 v[244:247], v145 offset:2064
	ds_read_b128 v[248:251], v145 offset:2080
	ds_read_b128 v[252:255], v145 offset:2096
	v_bfi_b32 v1, s10, v135, v18
	v_perm_b32 v121, v10, v135, s24
	v_cndmask_b32_e64 v18, v18, v1, s[0:1]
	v_cndmask_b32_e64 v10, v10, v121, s[0:1]
	s_add_i32 s22, s22, 0x80000
	s_add_i32 s11, s11, 1
	s_add_u32 s12, s12, 4
	s_addc_u32 s13, s13, 0
	v_add_u32_e32 v104, 0x400, v104
	v_add_u32_e32 v105, 0x800, v105
	v_add_u32_e32 v114, 2, v114
	s_cmp_eq_u32 s22, 0x898000
	s_waitcnt lgkmcnt(4)
	s_barrier
	ds_read_b128 v[232:235], v113
	ds_read_b128 v[236:239], v113 offset:1024
	s_waitcnt lgkmcnt(0)
	v_add_f32_e32 v0, v232, v233
	v_add_f32_e32 v1, v234, v235
	v_add_f32_e32 v121, v236, v237
	v_add_f32_e32 v144, v238, v239
	v_add_f32_e32 v0, v0, v1
	v_add_f32_e32 v121, v121, v144
	v_add_f32_e32 v0, v0, v121
	v_add_f32_e32 v0, s30, v0
	v_cvt_f16_f32_e32 v1, v0
	v_cvt_f16_f32_e32 v121, v0
	ds_write_b32 v106, v0
	v_add_u32_e32 v106, 4, v106
	v_permlane16_swap_b32_e32 v1, v121
	s_cbranch_scc0 .LBB1_4
